# W_o epilogue: all 16 residual loads issued up front, arithmetic, then the stores back to back (instead of 16 serialized load/store round trips), on top of the n=10 version
# speedup vs baseline: 1.0119x; 1.0079x over previous
; DI float bflo(unsigned u) { return __uint_as_float(u << 16); }
; DI float bfhi(unsigned u) { return __uint_as_float(u & 0xffff0000u); }
; DI int lane_id_now() { int l; asm volatile("v_mbcnt_lo_u32_b32 %0, -1, 0\n\tv_mbcnt_hi_u32_b32 %0, -1, %0" : "=v"(l)); return l; }
; template <class Cfg>
; DI void gemm256dma_unit(LDS_AS unsigned char* lds, const Cfg& cfg) {
;     ...
;     const int wid2 = wid, ln2 = lane_id_now(), wr2 = wid2 >> 2, wc2 = wid2 & 3, fr2 = ln2 & 15, fq2 = ln2 >> 4;
; #pragma unroll
;     for (int ai = 0; ai < 2; ++ai)
; #pragma unroll
;       for (int m = 0; m < 4; ++m)
; #pragma unroll
;         for (int bj = 0; bj < 2; ++bj)
;           cfg.epi(ai * 128 + wr2 * 64 + m * 16 + fr2, bj, wc2, fq2, acc[ai][bj][m][0], acc[ai][bj][m][1]);
;   DI void epi(int r, int bj, int wc, int fq, const f32x4& v0, const f32x4& v1) const {
;     const size_t o = (size_t)(pm * 256 + r) * 2048 + pn * 256 + 128 * bj + 64 * (wc >> 1) + 32 * (wc & 1) + 8 * fq;
;     const u32x4 rr = *(const u32x4*)(p.h0b + o);
;     const f32x4 h0 = {bflo(rr.x), bfhi(rr.x), bflo(rr.y), bfhi(rr.y)}, h1 = {bflo(rr.z), bfhi(rr.z), bflo(rr.w), bfhi(rr.w)};
;     const f32x4 x0 = h0 * DN_ALPHA + v0, x1 = h1 * DN_ALPHA + v1;
;     u32x4 pk; pk.x = pack2(x0[0], x0[1]); pk.y = pack2(x0[2], x0[3]); pk.z = pack2(x1[0], x1[1]); pk.w = pack2(x1[2], x1[3]);
;     *(u32x4*)(p.z1b + o) = pk;
;   }
.LBB0_1262:
	v_mbcnt_lo_u32_b32 v128, -1, 0
	v_mbcnt_hi_u32_b32 v128, -1, v128
	s_nop 0
	v_and_or_b32 v129, v128, 15, s21
	v_ashrrev_i32_e32 v128, 1, v128
	v_and_b32_e32 v130, -8, v128
	v_lshl_add_u32 v128, s10, 8, v129
	s_add_u32 s10, s18, s11
	v_ashrrev_i32_e32 v131, 31, v130
	v_ashrrev_i32_e32 v129, 31, v128
	s_addc_u32 s11, 0, 0
	v_lshl_add_u64 v[130:131], s[10:11], 0, v[130:131]
	v_readlane_b32 s12, v254, 56
	v_readlane_b32 s13, v254, 57
	v_lshl_add_u32 v134, v128, 11, v130
	v_lshlrev_b32_e32 v134, 1, v134
	v_add_u32_e32 v135, 0x10000, v134
	v_add_u32_e32 v136, 0x20000, v134
	v_add_u32_e32 v137, 0x30000, v134
	v_add_u32_e32 v138, 0x80000, v134
	v_add_u32_e32 v139, 0x90000, v134
	v_add_u32_e32 v140, 0xa0000, v134
	v_add_u32_e32 v141, 0xb0000, v134
	v_readlane_b32 s14, v254, 58
	v_readlane_b32 s15, v254, 59
	v_readlane_b32 s16, v254, 60
	v_readlane_b32 s17, v254, 61
	v_readlane_b32 s18, v254, 62
	v_readlane_b32 s19, v254, 63
	v_readlane_b32 s20, v255, 0
	v_readlane_b32 s21, v255, 1
	v_readlane_b32 s22, v255, 2
	v_readlane_b32 s23, v255, 3
	v_readlane_b32 s24, v255, 4
	v_readlane_b32 s25, v255, 5
	v_readlane_b32 s26, v255, 6
	v_readlane_b32 s27, v255, 7
	global_load_dwordx4 v[144:147], v134, s[12:13]
	global_load_dwordx4 v[148:151], v134, s[12:13] offset:256
	global_load_dwordx4 v[152:155], v135, s[12:13]
	global_load_dwordx4 v[156:159], v135, s[12:13] offset:256
	global_load_dwordx4 v[160:163], v136, s[12:13]
	global_load_dwordx4 v[164:167], v136, s[12:13] offset:256
	global_load_dwordx4 v[168:171], v137, s[12:13]
	global_load_dwordx4 v[172:175], v137, s[12:13] offset:256
	global_load_dwordx4 v[176:179], v138, s[12:13]
	global_load_dwordx4 v[180:183], v138, s[12:13] offset:256
	global_load_dwordx4 v[184:187], v139, s[12:13]
	global_load_dwordx4 v[188:191], v139, s[12:13] offset:256
	global_load_dwordx4 v[192:195], v140, s[12:13]
	global_load_dwordx4 v[196:199], v140, s[12:13] offset:256
	global_load_dwordx4 v[200:203], v141, s[12:13]
	global_load_dwordx4 v[204:207], v141, s[12:13] offset:256
	s_waitcnt vmcnt(15)
	v_lshlrev_b32_e32 v208, 16, v144
	v_and_b32_e32 v209, 0xffff0000, v144
	v_lshlrev_b32_e32 v210, 16, v145
	v_and_b32_e32 v211, 0xffff0000, v145
	v_lshlrev_b32_e32 v212, 16, v146
	v_and_b32_e32 v213, 0xffff0000, v146
	v_lshlrev_b32_e32 v214, 16, v147
	v_and_b32_e32 v215, 0xffff0000, v147
	v_pk_fma_f32 v[124:125], v[208:209], s[4:5], v[124:125] op_sel_hi:[1,0,1]
	v_pk_fma_f32 v[126:127], v[210:211], s[4:5], v[126:127] op_sel_hi:[1,0,1]
	v_pk_fma_f32 v[120:121], v[212:213], s[4:5], v[120:121] op_sel_hi:[1,0,1]
	v_pk_fma_f32 v[122:123], v[214:215], s[4:5], v[122:123] op_sel_hi:[1,0,1]
	v_cvt_pk_bf16_f32 v124, v124, v125
	v_cvt_pk_bf16_f32 v125, v126, v127
	v_cvt_pk_bf16_f32 v126, v120, v121
	v_cvt_pk_bf16_f32 v127, v122, v123
	s_waitcnt vmcnt(14)
	v_lshlrev_b32_e32 v208, 16, v148
	v_and_b32_e32 v209, 0xffff0000, v148
	v_lshlrev_b32_e32 v210, 16, v149
	v_and_b32_e32 v211, 0xffff0000, v149
	v_lshlrev_b32_e32 v212, 16, v150
	v_and_b32_e32 v213, 0xffff0000, v150
	v_lshlrev_b32_e32 v214, 16, v151
	v_and_b32_e32 v215, 0xffff0000, v151
	v_pk_fma_f32 v[116:117], v[208:209], s[4:5], v[116:117] op_sel_hi:[1,0,1]
	v_pk_fma_f32 v[118:119], v[210:211], s[4:5], v[118:119] op_sel_hi:[1,0,1]
	v_pk_fma_f32 v[112:113], v[212:213], s[4:5], v[112:113] op_sel_hi:[1,0,1]
	v_pk_fma_f32 v[114:115], v[214:215], s[4:5], v[114:115] op_sel_hi:[1,0,1]
	v_cvt_pk_bf16_f32 v116, v116, v117
	v_cvt_pk_bf16_f32 v117, v118, v119
	v_cvt_pk_bf16_f32 v118, v112, v113
	v_cvt_pk_bf16_f32 v119, v114, v115
	s_waitcnt vmcnt(13)
	v_lshlrev_b32_e32 v208, 16, v152
	v_and_b32_e32 v209, 0xffff0000, v152
	v_lshlrev_b32_e32 v210, 16, v153
	v_and_b32_e32 v211, 0xffff0000, v153
	v_lshlrev_b32_e32 v212, 16, v154
	v_and_b32_e32 v213, 0xffff0000, v154
	v_lshlrev_b32_e32 v214, 16, v155
	v_and_b32_e32 v215, 0xffff0000, v155
	v_pk_fma_f32 v[108:109], v[208:209], s[4:5], v[108:109] op_sel_hi:[1,0,1]
	v_pk_fma_f32 v[110:111], v[210:211], s[4:5], v[110:111] op_sel_hi:[1,0,1]
	v_pk_fma_f32 v[104:105], v[212:213], s[4:5], v[104:105] op_sel_hi:[1,0,1]
	v_pk_fma_f32 v[106:107], v[214:215], s[4:5], v[106:107] op_sel_hi:[1,0,1]
	v_cvt_pk_bf16_f32 v108, v108, v109
	v_cvt_pk_bf16_f32 v109, v110, v111
	v_cvt_pk_bf16_f32 v110, v104, v105
	v_cvt_pk_bf16_f32 v111, v106, v107
	s_waitcnt vmcnt(12)
	v_lshlrev_b32_e32 v208, 16, v156
	v_and_b32_e32 v209, 0xffff0000, v156
	v_lshlrev_b32_e32 v210, 16, v157
	v_and_b32_e32 v211, 0xffff0000, v157
	v_lshlrev_b32_e32 v212, 16, v158
	v_and_b32_e32 v213, 0xffff0000, v158
	v_lshlrev_b32_e32 v214, 16, v159
	v_and_b32_e32 v215, 0xffff0000, v159
	v_pk_fma_f32 v[100:101], v[208:209], s[4:5], v[100:101] op_sel_hi:[1,0,1]
	v_pk_fma_f32 v[102:103], v[210:211], s[4:5], v[102:103] op_sel_hi:[1,0,1]
	v_pk_fma_f32 v[96:97], v[212:213], s[4:5], v[96:97] op_sel_hi:[1,0,1]
	v_pk_fma_f32 v[98:99], v[214:215], s[4:5], v[98:99] op_sel_hi:[1,0,1]
	v_cvt_pk_bf16_f32 v100, v100, v101
	v_cvt_pk_bf16_f32 v101, v102, v103
	v_cvt_pk_bf16_f32 v102, v96, v97
	v_cvt_pk_bf16_f32 v103, v98, v99
	s_waitcnt vmcnt(11)
	v_lshlrev_b32_e32 v208, 16, v160
	v_and_b32_e32 v209, 0xffff0000, v160
	v_lshlrev_b32_e32 v210, 16, v161
	v_and_b32_e32 v211, 0xffff0000, v161
	v_lshlrev_b32_e32 v212, 16, v162
	v_and_b32_e32 v213, 0xffff0000, v162
	v_lshlrev_b32_e32 v214, 16, v163
	v_and_b32_e32 v215, 0xffff0000, v163
	v_pk_fma_f32 v[92:93], v[208:209], s[4:5], v[92:93] op_sel_hi:[1,0,1]
	v_pk_fma_f32 v[94:95], v[210:211], s[4:5], v[94:95] op_sel_hi:[1,0,1]
	v_pk_fma_f32 v[88:89], v[212:213], s[4:5], v[88:89] op_sel_hi:[1,0,1]
	v_pk_fma_f32 v[90:91], v[214:215], s[4:5], v[90:91] op_sel_hi:[1,0,1]
	v_cvt_pk_bf16_f32 v92, v92, v93
	v_cvt_pk_bf16_f32 v93, v94, v95
	v_cvt_pk_bf16_f32 v94, v88, v89
	v_cvt_pk_bf16_f32 v95, v90, v91
	s_waitcnt vmcnt(10)
; DI float bflo(unsigned u) { return __uint_as_float(u << 16); }
; DI float bfhi(unsigned u) { return __uint_as_float(u & 0xffff0000u); }
;   DI void epi(int r, int bj, int wc, int fq, const f32x4& v0, const f32x4& v1) const {
;     const size_t o = (size_t)(pm * 256 + r) * 2048 + pn * 256 + 128 * bj + 64 * (wc >> 1) + 32 * (wc & 1) + 8 * fq;
;     const u32x4 rr = *(const u32x4*)(p.h0b + o);
;     const f32x4 h0 = {bflo(rr.x), bfhi(rr.x), bflo(rr.y), bfhi(rr.y)}, h1 = {bflo(rr.z), bfhi(rr.z), bflo(rr.w), bfhi(rr.w)};
;     const f32x4 x0 = h0 * DN_ALPHA + v0, x1 = h1 * DN_ALPHA + v1;
;     u32x4 pk; pk.x = pack2(x0[0], x0[1]); pk.y = pack2(x0[2], x0[3]); pk.z = pack2(x1[0], x1[1]); pk.w = pack2(x1[2], x1[3]);
;     *(u32x4*)(p.z1b + o) = pk;
	v_lshlrev_b32_e32 v208, 16, v164
	v_and_b32_e32 v209, 0xffff0000, v164
	v_lshlrev_b32_e32 v210, 16, v165
	v_and_b32_e32 v211, 0xffff0000, v165
	v_lshlrev_b32_e32 v212, 16, v166
	v_and_b32_e32 v213, 0xffff0000, v166
	v_lshlrev_b32_e32 v214, 16, v167
	v_and_b32_e32 v215, 0xffff0000, v167
	v_pk_fma_f32 v[84:85], v[208:209], s[4:5], v[84:85] op_sel_hi:[1,0,1]
	v_pk_fma_f32 v[86:87], v[210:211], s[4:5], v[86:87] op_sel_hi:[1,0,1]
	v_pk_fma_f32 v[80:81], v[212:213], s[4:5], v[80:81] op_sel_hi:[1,0,1]
	v_pk_fma_f32 v[82:83], v[214:215], s[4:5], v[82:83] op_sel_hi:[1,0,1]
	v_cvt_pk_bf16_f32 v84, v84, v85
	v_cvt_pk_bf16_f32 v85, v86, v87
	v_cvt_pk_bf16_f32 v86, v80, v81
	v_cvt_pk_bf16_f32 v87, v82, v83
	s_waitcnt vmcnt(9)
	v_lshlrev_b32_e32 v208, 16, v168
	v_and_b32_e32 v209, 0xffff0000, v168
	v_lshlrev_b32_e32 v210, 16, v169
	v_and_b32_e32 v211, 0xffff0000, v169
	v_lshlrev_b32_e32 v212, 16, v170
	v_and_b32_e32 v213, 0xffff0000, v170
	v_lshlrev_b32_e32 v214, 16, v171
	v_and_b32_e32 v215, 0xffff0000, v171
	v_pk_fma_f32 v[76:77], v[208:209], s[4:5], v[76:77] op_sel_hi:[1,0,1]
	v_pk_fma_f32 v[78:79], v[210:211], s[4:5], v[78:79] op_sel_hi:[1,0,1]
	v_pk_fma_f32 v[72:73], v[212:213], s[4:5], v[72:73] op_sel_hi:[1,0,1]
	v_pk_fma_f32 v[74:75], v[214:215], s[4:5], v[74:75] op_sel_hi:[1,0,1]
	v_cvt_pk_bf16_f32 v76, v76, v77
	v_cvt_pk_bf16_f32 v77, v78, v79
	v_cvt_pk_bf16_f32 v78, v72, v73
	v_cvt_pk_bf16_f32 v79, v74, v75
	s_waitcnt vmcnt(8)
	v_lshlrev_b32_e32 v208, 16, v172
	v_and_b32_e32 v209, 0xffff0000, v172
	v_lshlrev_b32_e32 v210, 16, v173
	v_and_b32_e32 v211, 0xffff0000, v173
	v_lshlrev_b32_e32 v212, 16, v174
	v_and_b32_e32 v213, 0xffff0000, v174
	v_lshlrev_b32_e32 v214, 16, v175
	v_and_b32_e32 v215, 0xffff0000, v175
	v_pk_fma_f32 v[68:69], v[208:209], s[4:5], v[68:69] op_sel_hi:[1,0,1]
	v_pk_fma_f32 v[70:71], v[210:211], s[4:5], v[70:71] op_sel_hi:[1,0,1]
	v_pk_fma_f32 v[64:65], v[212:213], s[4:5], v[64:65] op_sel_hi:[1,0,1]
	v_pk_fma_f32 v[66:67], v[214:215], s[4:5], v[66:67] op_sel_hi:[1,0,1]
	v_cvt_pk_bf16_f32 v68, v68, v69
	v_cvt_pk_bf16_f32 v69, v70, v71
	v_cvt_pk_bf16_f32 v70, v64, v65
	v_cvt_pk_bf16_f32 v71, v66, v67
	s_waitcnt vmcnt(7)
	v_lshlrev_b32_e32 v208, 16, v176
	v_and_b32_e32 v209, 0xffff0000, v176
	v_lshlrev_b32_e32 v210, 16, v177
	v_and_b32_e32 v211, 0xffff0000, v177
	v_lshlrev_b32_e32 v212, 16, v178
	v_and_b32_e32 v213, 0xffff0000, v178
	v_lshlrev_b32_e32 v214, 16, v179
	v_and_b32_e32 v215, 0xffff0000, v179
	v_pk_fma_f32 v[60:61], v[208:209], s[4:5], v[60:61] op_sel_hi:[1,0,1]
	v_pk_fma_f32 v[62:63], v[210:211], s[4:5], v[62:63] op_sel_hi:[1,0,1]
	v_pk_fma_f32 v[56:57], v[212:213], s[4:5], v[56:57] op_sel_hi:[1,0,1]
	v_pk_fma_f32 v[58:59], v[214:215], s[4:5], v[58:59] op_sel_hi:[1,0,1]
	v_cvt_pk_bf16_f32 v60, v60, v61
	v_cvt_pk_bf16_f32 v61, v62, v63
	v_cvt_pk_bf16_f32 v62, v56, v57
	v_cvt_pk_bf16_f32 v63, v58, v59
	s_waitcnt vmcnt(6)
	v_lshlrev_b32_e32 v208, 16, v180
	v_and_b32_e32 v209, 0xffff0000, v180
	v_lshlrev_b32_e32 v210, 16, v181
	v_and_b32_e32 v211, 0xffff0000, v181
	v_lshlrev_b32_e32 v212, 16, v182
	v_and_b32_e32 v213, 0xffff0000, v182
	v_lshlrev_b32_e32 v214, 16, v183
	v_and_b32_e32 v215, 0xffff0000, v183
	v_pk_fma_f32 v[52:53], v[208:209], s[4:5], v[52:53] op_sel_hi:[1,0,1]
	v_pk_fma_f32 v[54:55], v[210:211], s[4:5], v[54:55] op_sel_hi:[1,0,1]
	v_pk_fma_f32 v[48:49], v[212:213], s[4:5], v[48:49] op_sel_hi:[1,0,1]
	v_pk_fma_f32 v[50:51], v[214:215], s[4:5], v[50:51] op_sel_hi:[1,0,1]
	v_cvt_pk_bf16_f32 v52, v52, v53
	v_cvt_pk_bf16_f32 v53, v54, v55
	v_cvt_pk_bf16_f32 v54, v48, v49
	v_cvt_pk_bf16_f32 v55, v50, v51
	s_waitcnt vmcnt(5)
	v_lshlrev_b32_e32 v208, 16, v184
	v_and_b32_e32 v209, 0xffff0000, v184
	v_lshlrev_b32_e32 v210, 16, v185
	v_and_b32_e32 v211, 0xffff0000, v185
	v_lshlrev_b32_e32 v212, 16, v186
	v_and_b32_e32 v213, 0xffff0000, v186
	v_lshlrev_b32_e32 v214, 16, v187
	v_and_b32_e32 v215, 0xffff0000, v187
	v_pk_fma_f32 v[44:45], v[208:209], s[4:5], v[44:45] op_sel_hi:[1,0,1]
	v_pk_fma_f32 v[46:47], v[210:211], s[4:5], v[46:47] op_sel_hi:[1,0,1]
	v_pk_fma_f32 v[40:41], v[212:213], s[4:5], v[40:41] op_sel_hi:[1,0,1]
	v_pk_fma_f32 v[42:43], v[214:215], s[4:5], v[42:43] op_sel_hi:[1,0,1]
	v_cvt_pk_bf16_f32 v44, v44, v45
	v_cvt_pk_bf16_f32 v45, v46, v47
	v_cvt_pk_bf16_f32 v46, v40, v41
	v_cvt_pk_bf16_f32 v47, v42, v43
	s_waitcnt vmcnt(4)
; DI float bflo(unsigned u) { return __uint_as_float(u << 16); }
; DI float bfhi(unsigned u) { return __uint_as_float(u & 0xffff0000u); }
; #define DENSE_UNIT(lds, cfg) gemm256dma_unit(lds, cfg)
; #define DENSE_UNIT(lds, cfg) gemm256_unit(lds, cfg)
;   DI void epi(int r, int bj, int wc, int fq, const f32x4& v0, const f32x4& v1) const {
;     const size_t o = (size_t)(pm * 256 + r) * 2048 + pn * 256 + 128 * bj + 64 * (wc >> 1) + 32 * (wc & 1) + 8 * fq;
;     const u32x4 rr = *(const u32x4*)(p.h0b + o);
;     const f32x4 h0 = {bflo(rr.x), bfhi(rr.x), bflo(rr.y), bfhi(rr.y)}, h1 = {bflo(rr.z), bfhi(rr.z), bflo(rr.w), bfhi(rr.w)};
;     const f32x4 x0 = h0 * DN_ALPHA + v0, x1 = h1 * DN_ALPHA + v1;
;     u32x4 pk; pk.x = pack2(x0[0], x0[1]); pk.y = pack2(x0[2], x0[3]); pk.z = pack2(x1[0], x1[1]); pk.w = pack2(x1[2], x1[3]);
;     *(u32x4*)(p.z1b + o) = pk;
;   }
;   for (int u = bid; u < 32 * 8; u += nb) {
;     const int uu = __builtin_amdgcn_readfirstlane(u);
;     CfgWo cfg{p, uu >> 3, uu & 7};
;     if (MODE == 0) DENSE_UNIT(lds, cfg); else gemm256_unit<CfgWo, MODE>(lds, cfg);
;   }
	v_lshlrev_b32_e32 v208, 16, v188
	v_and_b32_e32 v209, 0xffff0000, v188
	v_lshlrev_b32_e32 v210, 16, v189
	v_and_b32_e32 v211, 0xffff0000, v189
	v_lshlrev_b32_e32 v212, 16, v190
	v_and_b32_e32 v213, 0xffff0000, v190
	v_lshlrev_b32_e32 v214, 16, v191
	v_and_b32_e32 v215, 0xffff0000, v191
	v_pk_fma_f32 v[36:37], v[208:209], s[4:5], v[36:37] op_sel_hi:[1,0,1]
	v_pk_fma_f32 v[38:39], v[210:211], s[4:5], v[38:39] op_sel_hi:[1,0,1]
	v_pk_fma_f32 v[32:33], v[212:213], s[4:5], v[32:33] op_sel_hi:[1,0,1]
	v_pk_fma_f32 v[34:35], v[214:215], s[4:5], v[34:35] op_sel_hi:[1,0,1]
	v_cvt_pk_bf16_f32 v36, v36, v37
	v_cvt_pk_bf16_f32 v37, v38, v39
	v_cvt_pk_bf16_f32 v38, v32, v33
	v_cvt_pk_bf16_f32 v39, v34, v35
	s_waitcnt vmcnt(3)
	v_lshlrev_b32_e32 v208, 16, v192
	v_and_b32_e32 v209, 0xffff0000, v192
	v_lshlrev_b32_e32 v210, 16, v193
	v_and_b32_e32 v211, 0xffff0000, v193
	v_lshlrev_b32_e32 v212, 16, v194
	v_and_b32_e32 v213, 0xffff0000, v194
	v_lshlrev_b32_e32 v214, 16, v195
	v_and_b32_e32 v215, 0xffff0000, v195
	v_pk_fma_f32 v[28:29], v[208:209], s[4:5], v[28:29] op_sel_hi:[1,0,1]
	v_pk_fma_f32 v[30:31], v[210:211], s[4:5], v[30:31] op_sel_hi:[1,0,1]
	v_pk_fma_f32 v[24:25], v[212:213], s[4:5], v[24:25] op_sel_hi:[1,0,1]
	v_pk_fma_f32 v[26:27], v[214:215], s[4:5], v[26:27] op_sel_hi:[1,0,1]
	v_cvt_pk_bf16_f32 v28, v28, v29
	v_cvt_pk_bf16_f32 v29, v30, v31
	v_cvt_pk_bf16_f32 v30, v24, v25
	v_cvt_pk_bf16_f32 v31, v26, v27
	s_waitcnt vmcnt(2)
	v_lshlrev_b32_e32 v208, 16, v196
	v_and_b32_e32 v209, 0xffff0000, v196
	v_lshlrev_b32_e32 v210, 16, v197
	v_and_b32_e32 v211, 0xffff0000, v197
	v_lshlrev_b32_e32 v212, 16, v198
	v_and_b32_e32 v213, 0xffff0000, v198
	v_lshlrev_b32_e32 v214, 16, v199
	v_and_b32_e32 v215, 0xffff0000, v199
	v_pk_fma_f32 v[20:21], v[208:209], s[4:5], v[20:21] op_sel_hi:[1,0,1]
	v_pk_fma_f32 v[22:23], v[210:211], s[4:5], v[22:23] op_sel_hi:[1,0,1]
	v_pk_fma_f32 v[16:17], v[212:213], s[4:5], v[16:17] op_sel_hi:[1,0,1]
	v_pk_fma_f32 v[18:19], v[214:215], s[4:5], v[18:19] op_sel_hi:[1,0,1]
	v_cvt_pk_bf16_f32 v20, v20, v21
	v_cvt_pk_bf16_f32 v21, v22, v23
	v_cvt_pk_bf16_f32 v22, v16, v17
	v_cvt_pk_bf16_f32 v23, v18, v19
	s_waitcnt vmcnt(1)
	v_lshlrev_b32_e32 v208, 16, v200
	v_and_b32_e32 v209, 0xffff0000, v200
	v_lshlrev_b32_e32 v210, 16, v201
	v_and_b32_e32 v211, 0xffff0000, v201
	v_lshlrev_b32_e32 v212, 16, v202
	v_and_b32_e32 v213, 0xffff0000, v202
	v_lshlrev_b32_e32 v214, 16, v203
	v_and_b32_e32 v215, 0xffff0000, v203
	v_pk_fma_f32 v[12:13], v[208:209], s[4:5], v[12:13] op_sel_hi:[1,0,1]
	v_pk_fma_f32 v[14:15], v[210:211], s[4:5], v[14:15] op_sel_hi:[1,0,1]
	v_pk_fma_f32 v[8:9], v[212:213], s[4:5], v[8:9] op_sel_hi:[1,0,1]
	v_pk_fma_f32 v[10:11], v[214:215], s[4:5], v[10:11] op_sel_hi:[1,0,1]
	v_cvt_pk_bf16_f32 v12, v12, v13
	v_cvt_pk_bf16_f32 v13, v14, v15
	v_cvt_pk_bf16_f32 v14, v8, v9
	v_cvt_pk_bf16_f32 v15, v10, v11
	s_waitcnt vmcnt(0)
	v_lshlrev_b32_e32 v208, 16, v204
	v_and_b32_e32 v209, 0xffff0000, v204
	v_lshlrev_b32_e32 v210, 16, v205
	v_and_b32_e32 v211, 0xffff0000, v205
	v_lshlrev_b32_e32 v212, 16, v206
	v_and_b32_e32 v213, 0xffff0000, v206
	v_lshlrev_b32_e32 v214, 16, v207
	v_and_b32_e32 v215, 0xffff0000, v207
	v_pk_fma_f32 v[4:5], v[208:209], s[4:5], v[4:5] op_sel_hi:[1,0,1]
	v_pk_fma_f32 v[6:7], v[210:211], s[4:5], v[6:7] op_sel_hi:[1,0,1]
	v_pk_fma_f32 v[0:1], v[212:213], s[4:5], v[0:1] op_sel_hi:[1,0,1]
	v_pk_fma_f32 v[2:3], v[214:215], s[4:5], v[2:3] op_sel_hi:[1,0,1]
	v_cvt_pk_bf16_f32 v4, v4, v5
	v_cvt_pk_bf16_f32 v5, v6, v7
	v_cvt_pk_bf16_f32 v6, v0, v1
	v_cvt_pk_bf16_f32 v7, v2, v3
	global_store_dwordx4 v134, v[124:127], s[56:57]
	global_store_dwordx4 v134, v[116:119], s[56:57] offset:256
	global_store_dwordx4 v135, v[108:111], s[56:57]
	global_store_dwordx4 v135, v[100:103], s[56:57] offset:256
	global_store_dwordx4 v136, v[92:95], s[56:57]
	global_store_dwordx4 v136, v[84:87], s[56:57] offset:256
	global_store_dwordx4 v137, v[76:79], s[56:57]
	global_store_dwordx4 v137, v[68:71], s[56:57] offset:256
	global_store_dwordx4 v138, v[60:63], s[56:57]
	global_store_dwordx4 v138, v[52:55], s[56:57] offset:256
	global_store_dwordx4 v139, v[44:47], s[56:57]
	global_store_dwordx4 v139, v[36:39], s[56:57] offset:256
	global_store_dwordx4 v140, v[28:31], s[56:57]
	global_store_dwordx4 v140, v[20:23], s[56:57] offset:256
	global_store_dwordx4 v141, v[12:15], s[56:57]
	global_store_dwordx4 v141, v[4:7], s[56:57] offset:256
	s_add_i32 s9, s9, s96
	s_cmpk_lt_i32 s9, 0x100
	s_barrier
	s_cbranch_scc0 .LBB0_1269
